# v13 + each wave pre-touches its own first two codebook-fragment slices at kernel start (prologue loads hit L2)
# baseline (speedup 1.0000x reference)
_Z7k3_mainPKhPKfS2_S2_S2_PfS3_S3_:
	s_load_dwordx4 s[40:43], s[0:1], 0x0
	s_load_dwordx2 s[48:49], s[0:1], 0x10
	s_lshl_b32 s3, s2, 5
	s_and_b32 s3, s3, 0xe0
	s_lshr_b32 s2, s2, 3
	v_and_b32_e32 v128, 63, v0
	s_add_i32 s4, s3, s2
	s_waitcnt lgkmcnt(0)
	s_add_u32 s2, s40, 0x784000
	v_or_b32_e32 v134, 64, v128
	s_addc_u32 s3, s41, 0
	v_lshlrev_b32_e32 v98, 4, v128
	v_lshlrev_b32_e32 v1, 4, v134
	v_or_b32_e32 v133, 0x80, v128
	global_load_dwordx4 v[2:5], v98, s[2:3]
	global_load_dwordx4 v[6:9], v1, s[2:3]
	v_lshlrev_b32_e32 v1, 4, v133
	global_load_dwordx4 v[10:13], v1, s[2:3]
	v_or_b32_e32 v1, 0xc00, v98
	global_load_dwordx4 v[42:45], v1, s[2:3]
	s_load_dwordx2 s[2:3], s[0:1], 0x20
	v_lshrrev_b32_e32 v150, 6, v0
	s_lshl_b32 s33, s4, 4
	v_or_b32_e32 v66, s33, v150
	v_ashrrev_i32_e32 v67, 31, v66
	v_lshlrev_b64 v[14:15], 12, v[66:67]
	v_mov_b32_e32 v99, 0
	s_waitcnt lgkmcnt(0)
	v_lshl_add_u64 v[14:15], s[2:3], 0, v[14:15]
	v_lshl_add_u64 v[14:15], v[14:15], 0, v[98:99]
	global_load_dwordx4 v[54:57], v[14:15], off
	global_load_dwordx4 v[58:61], v[14:15], off offset:1024
	global_load_dwordx4 v[62:65], v[14:15], off offset:2048
	s_lshr_b32 s59, s33, 4
	s_and_b32 s59, s59, 31
	s_lshl_b32 s59, s59, 15
	s_add_u32 s59, s59, 0x787000
	s_add_u32 s68, s40, s59
	s_addc_u32 s69, s41, 0
	v_lshlrev_b32_e32 v207, 6, v0
	global_load_dword v207, v207, s[68:69]
	v_and_b32_e32 v206, 63, v0
	v_lshlrev_b32_e32 v206, 7, v206
	v_lshl_or_b32 v206, v150, 13, v206
	s_add_u32 s68, s40, 0x787000
	s_addc_u32 s69, s41, 0
	s_add_u32 s58, s68, 0x10000
	s_addc_u32 s59, s69, 0
	global_load_dword v205, v206, s[68:69]
	global_load_dword v204, v206, s[58:59]
	s_movk_i32 s4, 0xc00
	v_mov_b64_e32 v[16:17], s[42:43]
	v_mad_i64_i32 v[18:19], s[6:7], v66, s4, v[16:17]
	v_lshl_add_u64 v[18:19], v[18:19], 0, v[98:99]
	global_load_dwordx4 v[38:41], v[18:19], off
	global_load_dwordx4 v[34:37], v[18:19], off offset:1024
	global_load_dwordx4 v[30:33], v[18:19], off offset:2048
	global_load_dwordx4 v[68:71], v[14:15], off offset:3072
	v_mov_b32_e32 v50, v99
	v_mov_b32_e32 v51, v99
	v_mov_b32_e32 v52, v99
	v_mbcnt_lo_u32_b32 v1, -1, 0
	v_mov_b32_e32 v53, v99
	v_mbcnt_hi_u32_b32 v129, -1, v1
	v_and_b32_e32 v132, 64, v129
	v_xor_b32_e32 v1, 16, v129
	v_add_u32_e32 v130, 64, v132
	s_mov_b32 s5, 0xff61b1e6
	v_cmp_lt_i32_e32 vcc, v1, v130
	v_lshlrev_b32_e32 v135, 2, v128
	v_or_b32_e32 v146, 1, v135
	v_cndmask_b32_e32 v1, v129, v1, vcc
	v_or_b32_e32 v148, 2, v135
	v_or_b32_e32 v149, 3, v135
	v_or_b32_e32 v147, 0x100, v135
	v_or_b32_e32 v152, 0x101, v135
	v_or_b32_e32 v153, 0x102, v135
	v_or_b32_e32 v137, 0x103, v135
	v_or_b32_e32 v136, 0x200, v135
	v_or_b32_e32 v138, 0x201, v135
	v_or_b32_e32 v140, 0x202, v135
	v_or_b32_e32 v141, 0x203, v135
	v_or_b32_e32 v139, 0x300, v135
	v_or_b32_e32 v143, 0x301, v135
	v_or_b32_e32 v144, 0x302, v135
	s_add_u32 s50, s40, 0x780000
	s_addc_u32 s51, s41, 0
	v_or_b32_e32 v145, 0x303, v135
	v_lshl_add_u64 v[22:23], v[66:67], 2, s[50:51]
	global_load_dword v67, v[22:23], off
	v_lshlrev_b32_e32 v1, 2, v1
	v_or_b32_e32 v20, 8, v66
	v_ashrrev_i32_e32 v21, 31, v20
	v_mad_i64_i32 v[16:17], s[6:7], v20, s4, v[16:17]
	v_lshlrev_b64 v[18:19], 12, v[20:21]
	v_lshl_add_u64 v[46:47], v[16:17], 0, v[98:99]
	v_lshl_add_u64 v[16:17], s[2:3], 0, v[18:19]
	v_lshl_add_u64 v[48:49], v[16:17], 0, v[98:99]
	global_load_dwordx4 v[26:29], v[48:49], off
	global_load_dwordx4 v[22:25], v[48:49], off offset:1024
	global_load_dwordx4 v[18:21], v[48:49], off offset:2048
	global_load_dwordx4 v[14:17], v[48:49], off offset:3072
	s_waitcnt vmcnt(15)
	v_max_f32_e32 v5, v5, v5
	v_max_f32_e32 v4, v4, v4
	s_waitcnt vmcnt(14)
	v_max_f32_e32 v9, v9, v9
	v_max_f32_e32 v8, v8, v8
	s_waitcnt vmcnt(13)
	v_max_f32_e32 v13, v13, v13
	v_max_f32_e32 v12, v12, v12
	s_waitcnt vmcnt(12)
	v_max_f32_e32 v45, v45, v45
	v_max_f32_e32 v44, v44, v44
	v_max_f32_e32 v4, v4, v5
	v_max_f32_e32 v5, v8, v9
	v_max_f32_e32 v8, v12, v13
	v_max_f32_e32 v9, v44, v45
	v_max3_f32 v2, v2, v3, v4
	v_max3_f32 v3, v6, v7, v5
	v_max3_f32 v4, v10, v11, v8
	v_max3_f32 v5, v42, v43, v9
	v_max3_f32 v2, v2, 0, v3
	v_max3_f32 v2, v2, v4, v5
	s_waitcnt vmcnt(11)
	v_cmp_lt_f32_e32 vcc, s5, v54
	v_mov_b32_dpp v50, v2 row_ror:1 row_mask:0xf bank_mask:0xf
	v_max_f32_e32 v4, v50, v50
	v_max_f32_e32 v2, v2, v4
	v_cndmask_b32_e32 v3, 0, v135, vcc
	s_nop 0
	v_mov_b32_dpp v51, v2 row_ror:2 row_mask:0xf bank_mask:0xf
	v_max_f32_e32 v4, v51, v51
	v_max_f32_e32 v2, v2, v4
	s_nop 1
	v_mov_b32_dpp v52, v2 row_ror:4 row_mask:0xf bank_mask:0xf
	v_max_f32_e32 v4, v52, v52
	v_max_f32_e32 v2, v2, v4
	s_nop 1
	v_mov_b32_dpp v53, v2 row_ror:8 row_mask:0xf bank_mask:0xf
	v_max_f32_e32 v4, v53, v53
	v_max_f32_e32 v42, v2, v4
	v_max_f32_e32 v2, v54, v54
	v_max_f32_e32 v2, 0xff61b1e6, v2
	v_cmp_gt_f32_e32 vcc, v55, v2
	v_xor_b32_e32 v4, 32, v129
	ds_bpermute_b32 v43, v1, v42
	v_cndmask_b32_e32 v2, v2, v55, vcc
	v_cndmask_b32_e32 v3, v3, v146, vcc
	v_cmp_gt_f32_e32 vcc, v56, v2
	s_waitcnt lgkmcnt(0)
	v_max_f32_e32 v43, v43, v43
	v_cndmask_b32_e32 v2, v2, v56, vcc
	v_cndmask_b32_e32 v3, v3, v148, vcc
	v_cmp_gt_f32_e32 vcc, v57, v2
	v_max_f32_e32 v75, v42, v43
	v_mov_b64_e32 v[42:43], s[48:49]
	v_cndmask_b32_e32 v2, v2, v57, vcc
	v_cndmask_b32_e32 v3, v3, v149, vcc
	s_waitcnt vmcnt(10)
	v_cmp_gt_f32_e32 vcc, v58, v2
	s_nop 1
	v_cndmask_b32_e32 v2, v2, v58, vcc
	v_cndmask_b32_e32 v3, v3, v147, vcc
	v_cmp_gt_f32_e32 vcc, v59, v2
	s_nop 1
	v_cndmask_b32_e32 v2, v2, v59, vcc
	v_cndmask_b32_e32 v3, v3, v152, vcc
	v_cmp_gt_f32_e32 vcc, v60, v2
	s_nop 1
	v_cndmask_b32_e32 v2, v2, v60, vcc
	v_cndmask_b32_e32 v3, v3, v153, vcc
	v_cmp_gt_f32_e32 vcc, v61, v2
	s_nop 1
	v_cndmask_b32_e32 v2, v2, v61, vcc
	v_cndmask_b32_e32 v3, v3, v137, vcc
	s_waitcnt vmcnt(9)
	v_cmp_gt_f32_e32 vcc, v62, v2
	s_nop 1
	v_cndmask_b32_e32 v2, v2, v62, vcc
	v_cndmask_b32_e32 v3, v3, v136, vcc
	v_cmp_gt_f32_e32 vcc, v63, v2
	s_nop 1
	v_cndmask_b32_e32 v2, v2, v63, vcc
	v_cndmask_b32_e32 v3, v3, v138, vcc
	v_cmp_gt_f32_e32 vcc, v64, v2
	s_nop 1
	v_cndmask_b32_e32 v2, v2, v64, vcc
	v_cndmask_b32_e32 v3, v3, v140, vcc
	v_cmp_gt_f32_e32 vcc, v65, v2
	s_nop 1
	v_cndmask_b32_e32 v2, v2, v65, vcc
	v_cndmask_b32_e32 v3, v3, v141, vcc
	s_waitcnt vmcnt(5)
	v_cmp_gt_f32_e32 vcc, v68, v2
	s_nop 1
	v_cndmask_b32_e32 v2, v2, v68, vcc
	v_cndmask_b32_e32 v3, v3, v139, vcc
	v_cmp_gt_f32_e32 vcc, v69, v2
	s_nop 1
	v_cndmask_b32_e32 v2, v2, v69, vcc
	v_cndmask_b32_e32 v3, v3, v143, vcc
	v_cmp_gt_f32_e32 vcc, v70, v2
	s_nop 1
	v_cndmask_b32_e32 v2, v2, v70, vcc
	v_cndmask_b32_e32 v3, v3, v144, vcc
	v_cmp_gt_f32_e32 vcc, v71, v2
	s_nop 1
	v_cndmask_b32_e32 v45, v2, v71, vcc
	v_mov_b32_e32 v2, v99
	v_cndmask_b32_e32 v44, v3, v145, vcc
	v_max_f32_e32 v3, v45, v45
	v_mov_b32_dpp v2, v45 row_ror:1 row_mask:0xf bank_mask:0xf
	v_max_f32_e32 v2, v2, v2
	v_max_f32_e32 v2, v3, v2
	v_mov_b32_e32 v3, v99
	v_cmp_lt_i32_e32 vcc, v4, v130
	s_nop 0
	v_mov_b32_dpp v3, v2 row_ror:2 row_mask:0xf bank_mask:0xf
	v_max_f32_e32 v3, v3, v3
	v_max_f32_e32 v2, v2, v3
	v_mov_b32_e32 v3, v99
	v_cndmask_b32_e32 v4, v129, v4, vcc
	v_lshlrev_b32_e32 v151, 2, v4
	v_mov_b32_dpp v3, v2 row_ror:4 row_mask:0xf bank_mask:0xf
	v_max_f32_e32 v3, v3, v3
	v_max_f32_e32 v2, v2, v3
	v_mov_b32_e32 v3, v99
	ds_bpermute_b32 v76, v151, v75
	s_nop 0
	v_mov_b32_dpp v3, v2 row_ror:8 row_mask:0xf bank_mask:0xf
	v_max_f32_e32 v3, v3, v3
	v_max_f32_e32 v2, v2, v3
	ds_bpermute_b32 v3, v1, v2
	s_waitcnt lgkmcnt(0)
	v_max_f32_e32 v3, v3, v3
	v_max_f32_e32 v48, v2, v3
	ds_bpermute_b32 v49, v151, v48
	global_load_dwordx4 v[10:13], v[46:47], off
	global_load_dwordx4 v[6:9], v[46:47], off offset:1024
	global_load_dwordx4 v[2:5], v[46:47], off offset:2048
	s_waitcnt lgkmcnt(0)
	v_max_f32_e32 v46, v49, v49
	v_max_f32_e32 v74, v48, v46
	v_cmp_eq_f32_e32 vcc, v45, v74
	s_ff1_i32_b64 s2, vcc
	s_cmp_lg_u64 vcc, 0
	s_cselect_b32 s2, s2, 63
	v_or_b32_e32 v45, s2, v132
	v_lshlrev_b32_e32 v45, 2, v45
	ds_bpermute_b32 v44, v45, v44
	s_waitcnt lgkmcnt(0)
	v_mad_i64_i32 v[42:43], s[2:3], v44, s4, v[42:43]
	v_lshl_add_u64 v[72:73], v[42:43], 0, v[98:99]
	global_load_dwordx4 v[42:45], v[72:73], off
	global_load_dwordx4 v[46:49], v[72:73], off offset:1024
	global_load_dwordx4 v[50:53], v[72:73], off offset:2048
	v_max_f32_e32 v72, v76, v76
	v_max_f32_e32 v142, v75, v72
	s_waitcnt vmcnt(10)
	v_mul_f32_e32 v67, v142, v67
	s_mov_b32 s2, 0xf800000
	v_mul_f32_e32 v72, 0x4f800000, v67
	v_cmp_gt_f32_e32 vcc, s2, v67
	v_mad_i64_i32 v[90:91], s[2:3], v66, s4, 0
	s_nop 0
	v_cndmask_b32_e32 v67, v67, v72, vcc
	v_sqrt_f32_e32 v72, v67
	v_mov_b32_e32 v66, 0x1c000
	v_cmp_eq_u32_e64 s[2:3], 0, v128
	v_lshl_or_b32 v131, v150, 8, v66
	v_add_u32_e32 v73, -1, v72
	v_fma_f32 v75, -v73, v72, v67
	v_cmp_ge_f32_e64 s[4:5], 0, v75
	v_add_u32_e32 v75, 1, v72
	s_nop 0
	v_cndmask_b32_e64 v73, v72, v73, s[4:5]
	v_fma_f32 v72, -v75, v72, v67
	v_cmp_lt_f32_e64 s[4:5], 0, v72
	s_nop 1
	v_cndmask_b32_e64 v72, v73, v75, s[4:5]
	v_mul_f32_e32 v73, 0x37800000, v72
	v_cndmask_b32_e32 v72, v72, v73, vcc
	v_mov_b32_e32 v73, 0x260
	v_cmp_class_f32_e32 vcc, v67, v73
	s_nop 1
	v_cndmask_b32_e32 v67, v72, v67, vcc
	v_fmamk_f32 v67, v67, 0xbbb8cfc0, v74
	v_cmp_ge_f32_e64 s[36:37], v54, v67
	v_cmp_ge_f32_e64 s[34:35], v55, v67
	s_bcnt1_i32_b64 s4, s[36:37]
	s_bcnt1_i32_b64 s5, s[34:35]
	v_cmp_ge_f32_e64 s[30:31], v56, v67
	s_add_i32 s4, s4, s5
	s_bcnt1_i32_b64 s5, s[30:31]
	v_cmp_ge_f32_e64 s[28:29], v57, v67
	s_add_i32 s4, s4, s5
	s_bcnt1_i32_b64 s5, s[28:29]
	v_cmp_ge_f32_e64 s[26:27], v58, v67
	s_add_i32 s4, s4, s5
	s_bcnt1_i32_b64 s5, s[26:27]
	v_cmp_ge_f32_e64 s[24:25], v59, v67
	s_add_i32 s4, s4, s5
	s_bcnt1_i32_b64 s5, s[24:25]
	v_cmp_ge_f32_e64 s[22:23], v60, v67
	s_add_i32 s4, s4, s5
	s_bcnt1_i32_b64 s5, s[22:23]
	v_cmp_ge_f32_e64 s[20:21], v61, v67
	s_add_i32 s4, s4, s5
	s_bcnt1_i32_b64 s5, s[20:21]
	v_cmp_ge_f32_e64 s[18:19], v62, v67
	s_add_i32 s4, s4, s5
	s_bcnt1_i32_b64 s5, s[18:19]
	v_cmp_ge_f32_e64 s[16:17], v63, v67
	s_add_i32 s4, s4, s5
	s_bcnt1_i32_b64 s5, s[16:17]
	v_cmp_ge_f32_e64 s[14:15], v64, v67
	s_add_i32 s4, s4, s5
	s_bcnt1_i32_b64 s5, s[14:15]
	v_cmp_ge_f32_e64 s[12:13], v65, v67
	s_add_i32 s4, s4, s5
	s_bcnt1_i32_b64 s5, s[12:13]
	v_cmp_ge_f32_e64 s[10:11], v68, v67
	s_add_i32 s4, s4, s5
	s_bcnt1_i32_b64 s5, s[10:11]
	v_cmp_ge_f32_e64 s[8:9], v69, v67
	s_add_i32 s4, s4, s5
	s_bcnt1_i32_b64 s5, s[8:9]
	v_cmp_ge_f32_e64 s[6:7], v70, v67
	s_add_i32 s4, s4, s5
	s_bcnt1_i32_b64 s5, s[6:7]
	s_add_i32 s38, s4, s5
	v_cmp_ge_f32_e64 s[4:5], v71, v67
	s_bcnt1_i32_b64 s39, s[4:5]
	s_add_i32 s38, s38, s39
	s_cmpk_lt_u32 s38, 0x41
	s_cbranch_scc0 .LBB2_7
	s_cmp_gt_u32 s38, 1
	s_waitcnt vmcnt(0)
	v_mov_b64_e32 v[56:57], v[52:53]
	v_mov_b64_e32 v[54:55], v[50:51]
	v_mov_b64_e32 v[60:61], v[48:49]
	v_mov_b64_e32 v[58:59], v[46:47]
	v_mov_b64_e32 v[64:65], v[44:45]
	v_mov_b64_e32 v[62:63], v[42:43]
	s_cbranch_scc0 .LBB2_94
	v_cndmask_b32_e64 v54, 0, 1, s[36:37]
	s_mov_b32 s42, 0
	v_cmp_ne_u32_e32 vcc, 0, v54
	s_cbranch_vccz .LBB2_8
	v_mov_b32_e32 v54, 0x1c000
	v_lshl_or_b32 v54, v150, 8, v54
	s_branch .LBB2_5
